# DSA item set-up de-serialised: LDS zeroing moved in front of the wait for the key-rms row loads; on top of v27
# speedup vs baseline: 1.0087x; 1.0087x over previous
.LBB0_476:
	v_readlane_b32 s0, v254, 24
	s_waitcnt lgkmcnt(0)
	s_barrier
	v_mov_b32_e32 v0, s0
	ds_read_b32 v0, v0
	s_waitcnt lgkmcnt(0)
	v_readfirstlane_b32 s48, v0
	s_cmp_eq_u32 s48, -1
	s_cbranch_scc1 .LBB0_509
	s_lshr_b32 s19, s48, 8
	s_and_b32 s57, s48, 0xff
	s_cmpk_lt_u32 s57, 0x58
	s_mov_b64 s[0:1], -1
	s_cbranch_scc0 .LBB0_846
	s_and_b32 s0, s48, 0xfc
	s_cmp_lg_u32 s0, 4
	s_mov_b64 s[0:1], -1
	s_cbranch_scc0 .LBB0_830
	s_cmp_gt_u32 s57, 3
	s_cbranch_scc0 .LBB0_797
	s_cmp_gt_u32 s57, 55
	s_cbranch_scc0 .LBB0_767
	s_sub_i32 s0, s57, 56
	s_lshr_b32 s0, s0, 1
	s_sub_i32 s30, 15, s0
	s_and_b32 s18, s48, 1
	s_mov_b32 s44, s19
	v_mov_b32_e32 v0, v1
	s_ashr_i32 s45, s44, 31
	v_mbcnt_lo_u32_b32 v0, -1, v0
	v_mbcnt_hi_u32_b32 v42, -1, v0
	v_add_u32_e32 v2, s94, v42
	s_lshl_b64 s[0:1], s[44:45], 21
	v_readlane_b32 s12, v254, 34
	v_ashrrev_i32_e32 v4, 2, v2
	s_add_u32 s42, s12, s0
	v_readlane_b32 s0, v254, 35
	v_ashrrev_i32_e32 v5, 31, v4
	s_addc_u32 s43, s0, s1
	v_lshlrev_b64 v[4:5], 9, v[4:5]
	v_lshlrev_b32_e32 v0, 5, v42
	v_lshl_add_u64 v[4:5], s[42:43], 0, v[4:5]
	v_and_b32_e32 v0, 0x60, v0
	v_lshl_add_u64 v[8:9], v[4:5], 0, v[0:1]
	global_load_dwordx4 v[4:7], v[8:9], off offset:272
	s_nop 0
	global_load_dwordx4 v[8:11], v[8:9], off offset:256
	s_movk_i32 s0, 0x4000
	v_cmp_gt_i32_e32 vcc, s0, v2
	s_and_saveexec_b64 s[0:1], vcc
	s_movk_i32 s16, 0x3dff
	s_cbranch_execz .LBB0_494
	v_readlane_b32 s12, v253, 43
	s_nop 1
	v_lshl_add_u32 v204, v42, 2, s12
	v_readlane_b32 s12, v253, 44
	s_nop 1
	v_add_u32_e32 v205, s12, v42
	s_mov_b64 s[12:13], 0
.LBB0_493:
	v_add_u32_e32 v205, 0x200, v205
	v_cmp_lt_i32_e32 vcc, s16, v205
	ds_write_b32 v204, v1
	s_or_b64 s[12:13], vcc, s[12:13]
	v_add_u32_e32 v204, 0x800, v204
	s_andn2_b64 exec, exec, s[12:13]
	s_cbranch_execnz .LBB0_493
.LBB0_494:
	s_or_b64 exec, exec, s[0:1]
	s_movk_i32 s0, 0x2000
	v_lshlrev_b32_e32 v52, 4, v42
	v_cmp_gt_i32_e64 s[28:29], s0, v2
	s_and_saveexec_b64 s[0:1], s[28:29]
	s_movk_i32 s16, 0x1dff
	s_cbranch_execz .Lzero_end_a
	v_readlane_b32 s12, v253, 44
	s_nop 1
	v_add_u32_e32 v204, s12, v42
	v_readlane_b32 s12, v253, 45
	s_nop 1
	v_lshl_add_u32 v206, v42, 2, s12
	s_mov_b64 s[12:13], 0
.LBB0_496:
	v_add_u32_e32 v204, 0x200, v204
	v_cmp_lt_i32_e32 vcc, s16, v204
	ds_write_b32 v206, v1
	s_or_b64 s[12:13], vcc, s[12:13]
	v_add_u32_e32 v206, 0x800, v206
	s_andn2_b64 exec, exec, s[12:13]
	s_cbranch_execnz .LBB0_496
.Lzero_end_a:
	s_or_b64 exec, exec, s[0:1]
	v_cmp_eq_u32_e64 s[26:27], 0, v42
	s_waitcnt vmcnt(0)
	v_and_b32_e32 v3, 0xffff0000, v8
	v_lshlrev_b32_e32 v0, 16, v8
	v_mul_f32_e32 v3, v3, v3
	v_and_b32_e32 v8, 0xffff0000, v9
	v_fmac_f32_e32 v3, v0, v0
	v_lshlrev_b32_e32 v0, 16, v9
	v_mul_f32_e32 v8, v8, v8
	v_fmac_f32_e32 v8, v0, v0
	v_add_f32_e32 v0, v3, v8
	v_and_b32_e32 v8, 0xffff0000, v10
	v_lshlrev_b32_e32 v3, 16, v10
	v_mul_f32_e32 v8, v8, v8
	v_fmac_f32_e32 v8, v3, v3
	v_add_f32_e32 v0, v8, v0
	v_and_b32_e32 v8, 0xffff0000, v11
	v_lshlrev_b32_e32 v3, 16, v11
	v_mul_f32_e32 v8, v8, v8
	v_fmac_f32_e32 v8, v3, v3
	v_lshlrev_b32_e32 v3, 16, v4
	v_and_b32_e32 v4, 0xffff0000, v4
	v_mul_f32_e32 v4, v4, v4
	v_add_f32_e32 v0, v8, v0
	v_fmac_f32_e32 v4, v3, v3
	v_add_f32_e32 v0, v4, v0
	v_and_b32_e32 v4, 0xffff0000, v5
	v_lshlrev_b32_e32 v3, 16, v5
	v_mul_f32_e32 v4, v4, v4
	v_fmac_f32_e32 v4, v3, v3
	v_add_f32_e32 v0, v4, v0
	v_and_b32_e32 v4, 0xffff0000, v6
	v_lshlrev_b32_e32 v3, 16, v6
	v_mul_f32_e32 v4, v4, v4
	v_fmac_f32_e32 v4, v3, v3
	v_add_f32_e32 v0, v4, v0
	v_and_b32_e32 v4, 0xffff0000, v7
	v_lshlrev_b32_e32 v3, 16, v7
	v_mul_f32_e32 v4, v4, v4
	v_fmac_f32_e32 v4, v3, v3
	v_add_f32_e32 v0, v4, v0
	s_nop 1
	v_add_f32_dpp v0, v0, v0 quad_perm:[1,0,3,2] row_mask:0xf bank_mask:0xf bound_ctrl:1
	s_nop 1
	v_add_f32_dpp v0, v0, v0 quad_perm:[2,3,0,1] row_mask:0xf bank_mask:0xf bound_ctrl:1
	s_nop 1
	v_add_f32_dpp v0, v0, v0 row_half_mirror row_mask:0xf bank_mask:0xf bound_ctrl:1
	s_nop 1
	v_add_f32_dpp v0, v0, v0 row_mirror row_mask:0xf bank_mask:0xf bound_ctrl:1
	v_mov_b32_e32 v3, v0
	s_nop 1
	v_permlane16_swap_b32_e32 v0, v3
	v_add_f32_e32 v0, v0, v3
	v_mov_b32_e32 v3, v0
	s_nop 1
	v_permlane32_swap_b32_e32 v0, v3
	s_and_saveexec_b64 s[0:1], s[26:27]
	s_cbranch_execz .LBB0_483
	v_readlane_b32 s12, v252, 18
	v_add_f32_e32 v0, v0, v3
	s_nop 0
	v_mov_b32_e32 v3, s12
	ds_write_b32 v3, v0

.LBB0_491:
	s_or_b64 exec, exec, s[0:1]
	s_movk_i32 s0, 0x2000
	v_cmp_gt_i32_e64 s[28:29], s0, v2

.LBB0_767:
	s_and_b64 vcc, exec, s[0:1]
	s_cbranch_vccz .LBB0_796
	s_sub_i32 s30, 0x47, s57
	s_mov_b32 s18, 2
	s_mov_b32 s44, s19
	v_mov_b32_e32 v0, v1
	s_ashr_i32 s45, s44, 31
	v_mbcnt_lo_u32_b32 v0, -1, v0
	v_mbcnt_hi_u32_b32 v42, -1, v0
	v_add_u32_e32 v2, s94, v42
	s_lshl_b64 s[0:1], s[44:45], 21
	v_readlane_b32 s12, v254, 34
	v_ashrrev_i32_e32 v4, 2, v2
	s_add_u32 s42, s12, s0
	v_readlane_b32 s0, v254, 35
	v_ashrrev_i32_e32 v5, 31, v4
	s_addc_u32 s43, s0, s1
	v_lshlrev_b64 v[4:5], 9, v[4:5]
	v_lshlrev_b32_e32 v0, 5, v42
	v_lshl_add_u64 v[4:5], s[42:43], 0, v[4:5]
	v_and_b32_e32 v0, 0x60, v0
	v_lshl_add_u64 v[8:9], v[4:5], 0, v[0:1]
	global_load_dwordx4 v[4:7], v[8:9], off offset:272
	s_nop 0
	global_load_dwordx4 v[8:11], v[8:9], off offset:256
	s_movk_i32 s0, 0x4000
	v_cmp_gt_i32_e32 vcc, s0, v2
	s_and_saveexec_b64 s[0:1], vcc
	s_movk_i32 s16, 0x3dff
	s_cbranch_execz .LBB0_781
	v_readlane_b32 s12, v253, 43
	s_nop 1
	v_lshl_add_u32 v204, v42, 2, s12
	v_readlane_b32 s12, v253, 44
	s_nop 1
	v_add_u32_e32 v205, s12, v42
	s_mov_b64 s[12:13], 0
